# P + attention main loop prefetches the third K k-step fragments across the barrier into spare VGPRs v222-237 (KPF 2->3): 4 ds_read_b128 move from the MFMA segment to the softmax segment's tail
# baseline (speedup 1.0000x reference)
.LBB0_1608:
	s_and_b32 s2, s4, 0x3fffffc0
	s_lshl_b32 s2, s2, 2
	s_add_i32 s13, s2, 0
	v_and_b32_e32 v193, 63, v192
	v_exp_f32_e32 v159, v81
	v_exp_f32_e32 v167, v97
	v_exp_f32_e32 v158, v80
	v_exp_f32_e32 v156, v82
	v_exp_f32_e32 v157, v83
	v_exp_f32_e32 v166, v96
	v_exp_f32_e32 v164, v98
	v_exp_f32_e32 v165, v99
	v_exp_f32_e32 v154, v84
	v_exp_f32_e32 v155, v85
	v_exp_f32_e32 v162, v100
	v_exp_f32_e32 v163, v101
	v_exp_f32_e32 v152, v86
	v_exp_f32_e32 v153, v87
	v_exp_f32_e32 v160, v102
	v_exp_f32_e32 v161, v103
	v_exp_f32_e32 v150, v88
	v_exp_f32_e32 v151, v89
	v_exp_f32_e32 v104, v104
	v_exp_f32_e32 v105, v105
	v_max_f32_e32 v65, v159, v167
	v_exp_f32_e32 v148, v90
	v_exp_f32_e32 v149, v91
	v_exp_f32_e32 v102, v106
	v_exp_f32_e32 v103, v107
	v_max3_f32 v65, v158, v166, v65
	v_max_f32_e32 v66, v156, v164
	v_max_f32_e32 v67, v157, v165
	v_exp_f32_e32 v146, v92
	v_exp_f32_e32 v147, v93
	v_exp_f32_e32 v100, v108
	v_exp_f32_e32 v101, v109
	v_max3_f32 v65, v65, v66, v67
	v_max_f32_e32 v66, v154, v162
	v_max_f32_e32 v67, v155, v163
	v_exp_f32_e32 v144, v94
	v_exp_f32_e32 v145, v95
	v_exp_f32_e32 v98, v110
	v_exp_f32_e32 v99, v111
	v_max3_f32 v65, v65, v66, v67
	v_max_f32_e32 v66, v152, v160
	v_max_f32_e32 v67, v153, v161
	v_max3_f32 v65, v65, v66, v67
	v_max_f32_e32 v66, v150, v104
	v_max_f32_e32 v67, v151, v105
	v_max3_f32 v65, v65, v66, v67
	v_max_f32_e32 v66, v148, v102
	v_max_f32_e32 v67, v149, v103
	v_max3_f32 v65, v65, v66, v67
	v_max_f32_e32 v66, v146, v100
	v_max_f32_e32 v67, v147, v101
	v_max3_f32 v65, v65, v66, v67
	v_max_f32_e32 v66, v144, v98
	v_max_f32_e32 v67, v145, v99
	v_max3_f32 v65, v65, v66, v67
	v_mov_b32_e32 v66, v65
	s_nop 1
	v_permlane32_swap_b32_e32 v65, v66
	v_max_f32_e32 v66, v66, v66
	v_max_f32_e32 v65, v65, v65
	v_max_f32_e32 v65, v65, v66
	v_log_f32_e32 v65, v65
	v_cmp_gt_u32_e64 s[2:3], 32, v193
	v_lshl_add_u32 v196, v194, 2, s13
	v_add_f32_e32 v65, 0xc0400000, v65
	v_max_f32_e32 v65, 0, v65
	v_ceil_f32_e32 v65, v65
	v_exp_f32_e64 v106, -v65
	s_and_saveexec_b64 s[4:5], s[2:3]
	ds_write_b32 v196, v106 offset:60544
	s_or_b64 exec, exec, s[4:5]
	v_pk_mul_f32 v[66:67], v[158:159], v[106:107] op_sel_hi:[1,0]
	v_pk_mul_f32 v[82:83], v[166:167], v[106:107] op_sel_hi:[1,0]
	v_pk_mul_f32 v[68:69], v[156:157], v[106:107] op_sel_hi:[1,0]
	v_pk_mul_f32 v[84:85], v[164:165], v[106:107] op_sel_hi:[1,0]
	v_pk_mul_f32 v[70:71], v[154:155], v[106:107] op_sel_hi:[1,0]
	v_pk_mul_f32 v[86:87], v[162:163], v[106:107] op_sel_hi:[1,0]
	v_pk_mul_f32 v[72:73], v[152:153], v[106:107] op_sel_hi:[1,0]
	v_pk_mul_f32 v[88:89], v[160:161], v[106:107] op_sel_hi:[1,0]
	v_pk_mul_f32 v[74:75], v[150:151], v[106:107] op_sel_hi:[1,0]
	v_pk_mul_f32 v[90:91], v[104:105], v[106:107] op_sel_hi:[1,0]
	v_pk_mul_f32 v[76:77], v[148:149], v[106:107] op_sel_hi:[1,0]
	v_pk_mul_f32 v[92:93], v[102:103], v[106:107] op_sel_hi:[1,0]
	v_pk_mul_f32 v[78:79], v[146:147], v[106:107] op_sel_hi:[1,0]
	v_pk_mul_f32 v[94:95], v[100:101], v[106:107] op_sel_hi:[1,0]
	v_pk_mul_f32 v[80:81], v[144:145], v[106:107] op_sel_hi:[1,0]
	v_pk_mul_f32 v[96:97], v[98:99], v[106:107] op_sel_hi:[1,0]
	v_add_f32_e32 v107, 0, v158
	v_add_f32_e32 v107, v159, v107
	v_add_f32_e32 v107, v156, v107
	v_add_f32_e32 v107, v157, v107
	v_add_f32_e32 v107, v154, v107
	v_add_f32_e32 v107, v155, v107
	v_add_f32_e32 v107, v152, v107
	v_add_f32_e32 v107, v153, v107
	v_add_f32_e32 v107, v150, v107
	v_add_f32_e32 v107, v151, v107
	v_add_f32_e32 v107, v148, v107
	v_add_f32_e32 v107, v149, v107
	v_add_f32_e32 v107, v146, v107
	v_add_f32_e32 v107, v147, v107
	v_add_f32_e32 v107, v144, v107
	v_add_f32_e32 v107, v145, v107
	v_add_f32_e32 v107, v166, v107
	v_add_f32_e32 v107, v167, v107
	v_add_f32_e32 v107, v164, v107
	v_add_f32_e32 v107, v165, v107
	v_add_f32_e32 v107, v162, v107
	v_add_f32_e32 v107, v163, v107
	v_add_f32_e32 v107, v160, v107
	v_add_f32_e32 v107, v161, v107
	v_add_f32_e32 v104, v104, v107
	v_add_f32_e32 v104, v105, v104
	v_add_f32_e32 v102, v102, v104
	v_add_f32_e32 v102, v103, v102
	v_add_f32_e32 v100, v100, v102
	v_add_f32_e32 v100, v101, v100
	v_add_f32_e32 v98, v98, v100
	v_lshrrev_b32_e32 v100, 3, v192
	v_and_b32_e32 v195, 4, v100
	s_waitcnt lgkmcnt(0)
	v_lshl_add_u32 v197, v195, 2, s13
	ds_read_b128 v[100:103], v197 offset:60608
	ds_read_b128 v[108:111], v197 offset:60640
	ds_read_b128 v[206:209], v197 offset:60544
	ds_read_b128 v[144:147], v197 offset:60576
	v_cvt_pk_fp8_f32 v112, v66, v67
	v_cvt_pk_fp8_f32 v113, v70, v71
	v_cvt_pk_fp8_f32 v114, v74, v75
	v_cvt_pk_fp8_f32 v115, v78, v79
	s_waitcnt lgkmcnt(0)
	v_pk_mul_f32 v[4:5], v[4:5], v[144:145]
	v_pk_mul_f32 v[6:7], v[6:7], v[146:147]
	v_pk_mul_f32 v[20:21], v[20:21], v[144:145]
	v_pk_mul_f32 v[22:23], v[22:23], v[146:147]
	v_pk_mul_f32 v[36:37], v[36:37], v[144:145]
	v_pk_mul_f32 v[38:39], v[38:39], v[146:147]
	v_pk_mul_f32 v[52:53], v[52:53], v[144:145]
	v_pk_mul_f32 v[54:55], v[54:55], v[146:147]
	ds_read_b128 v[222:225], v204 offset:33920
	ds_read_b128 v[226:229], v204 offset:33936
	ds_read_b128 v[230:233], v204 offset:40576
	ds_read_b128 v[234:237], v204 offset:40592
	ds_read_b128 v[168:171], v204 offset:33792
	ds_read_b128 v[172:175], v204 offset:33808
	ds_read_b128 v[160:163], v204 offset:40448
	ds_read_b128 v[164:167], v204 offset:40464
	ds_read_b128 v[152:155], v204 offset:33856
	ds_read_b128 v[156:159], v204 offset:33872
	ds_read_b128 v[144:147], v204 offset:40512
	ds_read_b128 v[148:151], v204 offset:40528
	v_cvt_pk_fp8_f32 v116, v82, v83
	v_cvt_pk_fp8_f32 v117, v86, v87
	v_cvt_pk_fp8_f32 v118, v90, v91
	v_cvt_pk_fp8_f32 v119, v94, v95
	v_cvt_pk_fp8_f32 v112, v68, v69 op_sel:[0,0,1]
	v_cvt_pk_fp8_f32 v113, v72, v73 op_sel:[0,0,1]
	v_cvt_pk_fp8_f32 v114, v76, v77 op_sel:[0,0,1]
	v_cvt_pk_fp8_f32 v115, v80, v81 op_sel:[0,0,1]
	v_cvt_pk_fp8_f32 v116, v84, v85 op_sel:[0,0,1]
	v_cvt_pk_fp8_f32 v117, v88, v89 op_sel:[0,0,1]
	v_cvt_pk_fp8_f32 v118, v92, v93 op_sel:[0,0,1]
	v_cvt_pk_fp8_f32 v119, v96, v97 op_sel:[0,0,1]
	v_mul_f32_e32 v187, 0, v106
	v_add_f32_e32 v98, v99, v98
	v_pk_mul_f32 v[12:13], v[12:13], v[108:109]
	v_pk_mul_f32 v[8:9], v[8:9], v[100:101]
	v_pk_mul_f32 v[14:15], v[14:15], v[110:111]
	v_pk_mul_f32 v[10:11], v[10:11], v[102:103]
	v_pk_mul_f32 v[2:3], v[2:3], v[208:209]
	v_pk_mul_f32 v[0:1], v[0:1], v[206:207]
	v_pk_mul_f32 v[28:29], v[28:29], v[108:109]
	v_pk_mul_f32 v[24:25], v[24:25], v[100:101]
	v_pk_mul_f32 v[30:31], v[30:31], v[110:111]
	v_pk_mul_f32 v[26:27], v[26:27], v[102:103]
	v_pk_mul_f32 v[18:19], v[18:19], v[208:209]
	v_pk_mul_f32 v[16:17], v[16:17], v[206:207]
	v_pk_mul_f32 v[44:45], v[44:45], v[108:109]
	v_pk_mul_f32 v[40:41], v[40:41], v[100:101]
	v_pk_mul_f32 v[46:47], v[46:47], v[110:111]
	v_pk_mul_f32 v[42:43], v[42:43], v[102:103]
	v_pk_mul_f32 v[34:35], v[34:35], v[208:209]
	v_pk_mul_f32 v[32:33], v[32:33], v[206:207]
	v_pk_mul_f32 v[60:61], v[60:61], v[108:109]
	v_pk_mul_f32 v[56:57], v[56:57], v[100:101]
	v_pk_mul_f32 v[62:63], v[62:63], v[110:111]
	v_pk_mul_f32 v[58:59], v[58:59], v[102:103]
	v_pk_mul_f32 v[50:51], v[50:51], v[208:209]
	v_pk_mul_f32 v[48:49], v[48:49], v[206:207]
	v_mul_f32_e32 v98, v98, v106
	v_add_f32_e32 v187, v187, v98
	s_nop 0
	v_cndmask_b32_e64 v66, 0, 1, s[6:7]
	v_cmp_ne_u32_e64 s[4:5], 1, v66
	s_andn2_b64 vcc, exec, s[6:7]
	s_cbranch_vccnz .LBB0_1612
	s_waitcnt lgkmcnt(0)
	s_barrier

.LBB0_1614:
	s_mul_i32 s14, s13, 0x3400
	s_and_b32 s7, 1, s18
	s_add_i32 s14, s14, 0
	s_andn2_b32 s15, 1, s18
	s_mul_i32 s6, s17, 0x3400
	s_cmpk_lt_u32 s18, 0xfc
	s_cselect_b32 s21, s20, 0x2fd000
	s_cmp_eq_u32 s7, 1
	v_add_u32_e32 v96, s14, v199
	s_waitcnt lgkmcnt(6)
	v_mfma_scale_f32_32x32x64_f8f6f4 v[80:95], v[168:175], v[136:143], v[64:79], v191, v190 op_sel_hi:[0,0,0]
	s_waitcnt vmcnt(2)
	ds_write_b128 v96, v[180:183] offset:20480
	v_add_u32_e32 v96, s14, v200
	s_mulk_i32 s15, 0x2800
	s_waitcnt vmcnt(1)
	ds_write_b64 v96, v[188:189] offset:28672
	v_add_u32_e32 v96, s15, v205
	s_mov_b32 s39, s31
	s_waitcnt vmcnt(0)
	ds_write_b128 v96, v[176:179]
	buffer_load_dwordx4 v[180:183], v203, s[28:31], s21 offen
	buffer_load_dwordx2 v[188:189], v202, s[28:31], s21 offen
	buffer_load_dwordx4 v[176:179], v203, s[36:39], s19 offen
	s_cselect_b32 s6, 0x2800, 0
	v_add_u32_e32 v186, s6, v198
	s_waitcnt lgkmcnt(7)
	v_mfma_scale_f32_32x32x64_f8f6f4 v[96:111], v[160:167], v[136:143], v[64:79], v191, v190 op_sel_hi:[0,0,0]
	s_waitcnt lgkmcnt(5)
	v_mfma_scale_f32_32x32x64_f8f6f4 v[80:95], v[152:159], v[128:135], v[80:95], v191, v190 op_sel_hi:[0,0,0]
	ds_read_b128 v[152:155], v186
	ds_read_b128 v[156:159], v186 offset:16
	ds_read_b128 v[206:209], v186 offset:2560
	ds_read_b128 v[210:213], v186 offset:2576
	s_waitcnt lgkmcnt(7)
	v_mfma_scale_f32_32x32x64_f8f6f4 v[96:111], v[144:151], v[128:135], v[96:111], v191, v190 op_sel_hi:[0,0,0]
	ds_read_b128 v[144:147], v186 offset:5120
	ds_read_b128 v[148:151], v186 offset:5136
	ds_read_b128 v[214:217], v186 offset:7680
	ds_read_b128 v[218:221], v186 offset:7696
	v_mfma_scale_f32_32x32x64_f8f6f4 v[80:95], v[222:229], v[120:127], v[80:95], v191, v190 op_sel_hi:[0,0,0]
	v_mfma_scale_f32_32x32x64_f8f6f4 v[96:111], v[230:237], v[120:127], v[96:111], v191, v190 op_sel_hi:[0,0,0]
	s_waitcnt lgkmcnt(6)
	v_mfma_f32_32x32x64_f8f6f4 v[0:15], v[112:119], v[152:159], v[0:15]
	s_waitcnt lgkmcnt(4)
	v_mfma_f32_32x32x64_f8f6f4 v[16:31], v[112:119], v[206:213], v[16:31]
	s_waitcnt lgkmcnt(2)
	v_mfma_f32_32x32x64_f8f6f4 v[32:47], v[112:119], v[144:151], v[32:47]
	s_waitcnt lgkmcnt(0)
	v_mfma_f32_32x32x64_f8f6f4 v[48:63], v[112:119], v[214:221], v[48:63]
	v_cndmask_b32_e64 v144, 0, 1, s[46:47]
	v_cmp_ne_u32_e64 s[6:7], 1, v144
	s_andn2_b64 vcc, exec, s[46:47]
	s_cbranch_vccnz .LBB0_1616
	s_barrier

.LBB0_1617:
	s_mul_i32 s14, s16, 0x3400
	v_add_u32_e32 v148, s14, v204
	ds_read_b128 v[222:225], v148 offset:20608
	ds_read_b128 v[226:229], v148 offset:20624
	ds_read_b128 v[230:233], v148 offset:27264
	ds_read_b128 v[234:237], v148 offset:27280
	ds_read_b128 v[168:171], v148 offset:20480
	ds_read_b128 v[172:175], v148 offset:20496
	ds_read_b128 v[160:163], v148 offset:27136
	ds_read_b128 v[164:167], v148 offset:27152
	ds_read_b128 v[152:155], v148 offset:20544
	ds_read_b128 v[156:159], v148 offset:20560
	ds_read_b128 v[144:147], v148 offset:27200
	ds_read_b128 v[148:151], v148 offset:27216
	v_cvt_pk_fp8_f32 v112, v80, v81
	v_cvt_pk_fp8_f32 v113, v84, v85
	v_cvt_pk_fp8_f32 v114, v88, v89
	v_cvt_pk_fp8_f32 v115, v92, v93
	v_cvt_pk_fp8_f32 v116, v96, v97
	v_cvt_pk_fp8_f32 v117, v100, v101
	v_cvt_pk_fp8_f32 v118, v104, v105
	v_cvt_pk_fp8_f32 v119, v108, v109
	v_cvt_pk_fp8_f32 v112, v82, v83 op_sel:[0,0,1]
	v_cvt_pk_fp8_f32 v113, v86, v87 op_sel:[0,0,1]
	v_cvt_pk_fp8_f32 v114, v90, v91 op_sel:[0,0,1]
	v_cvt_pk_fp8_f32 v115, v94, v95 op_sel:[0,0,1]
	v_cvt_pk_fp8_f32 v116, v98, v99 op_sel:[0,0,1]
	v_cvt_pk_fp8_f32 v117, v102, v103 op_sel:[0,0,1]
	v_cvt_pk_fp8_f32 v118, v106, v107 op_sel:[0,0,1]
	v_cvt_pk_fp8_f32 v119, v110, v111 op_sel:[0,0,1]
	v_add_f32_e32 v187, v187, v186
	s_nop 0
	s_and_b64 vcc, exec, s[4:5]
	s_cbranch_vccnz .LBB0_1613
	s_waitcnt lgkmcnt(0)
	s_barrier
	s_branch .LBB0_1613
